# v39
# speedup vs baseline: 1.0005x; 1.0005x over previous
_Z8k_layer1PKiS0_PKfS2_PK15HIP_vector_typeIjLj4EEPKDv8_DF16_S9_S2_S2_S2_PDF16_PfSB_:
	s_load_dwordx2 s[14:15], s[0:1], 0x48
	s_load_dwordx8 s[4:11], s[0:1], 0x28
	s_load_dwordx2 s[56:57], s[0:1], 0x0
	v_readfirstlane_b32 s13, v0
	s_lshr_b32 s12, s13, 6
	v_and_b32_e32 v178, 63, v0
	v_lshl_or_b32 v2, s12, 10, v178
	v_ashrrev_i32_e32 v3, 31, v2
	v_lshlrev_b64 v[4:5], 4, v[2:3]
	s_lshl_b32 s16, s2, 5
	s_lshl_b32 s17, s12, 3
	s_add_i32 s16, s16, s17
	v_min_i32_e32 v1, 8, v178
	v_add_u32_e32 v1, s16, v1
	v_min_i32_e32 v1, 0xc350, v1
	v_lshlrev_b32_e32 v1, 2, v1
	s_waitcnt lgkmcnt(0)
	global_load_dword v236, v1, s[56:57]
	v_lshl_add_u64 v[6:7], s[6:7], 0, v[4:5]
	s_movk_i32 s3, 0x1000
	v_add_co_u32_e32 v8, vcc, s3, v6
	s_movk_i32 s6, 0x2000
	s_nop 0
	v_addc_co_u32_e32 v9, vcc, 0, v7, vcc
	v_add_co_u32_e32 v10, vcc, s6, v6
	s_movk_i32 s6, 0x3000
	s_nop 0
	v_addc_co_u32_e32 v11, vcc, 0, v7, vcc
	global_load_dwordx4 v[32:35], v[6:7], off
	global_load_dwordx4 v[36:39], v[6:7], off offset:1024
	global_load_dwordx4 v[40:43], v[6:7], off offset:2048
	global_load_dwordx4 v[44:47], v[6:7], off offset:3072
	v_add_co_u32_e32 v6, vcc, s6, v6
	v_lshl_add_u64 v[4:5], s[4:5], 0, v[4:5]
	s_nop 0
	v_addc_co_u32_e32 v7, vcc, 0, v7, vcc
	v_or_b32_e32 v2, 0x200, v2
	global_load_dwordx4 v[48:51], v[8:9], off offset:1024
	global_load_dwordx4 v[52:55], v[8:9], off offset:2048
	global_load_dwordx4 v[56:59], v[10:11], off offset:-4096
	global_load_dwordx4 v[60:63], v[10:11], off
	global_load_dwordx4 v[64:67], v[10:11], off offset:1024
	global_load_dwordx4 v[68:71], v[10:11], off offset:2048
	global_load_dwordx4 v[72:75], v[10:11], off offset:3072
	global_load_dwordx4 v[76:79], v[8:9], off offset:3072
	global_load_dwordx4 v[80:83], v[6:7], off
	global_load_dwordx4 v[84:87], v[6:7], off offset:1024
	global_load_dwordx4 v[88:91], v[6:7], off offset:2048
	global_load_dwordx4 v[92:95], v[6:7], off offset:3072
	v_add_co_u32_e32 v6, vcc, s3, v4
	v_ashrrev_i32_e32 v3, 31, v2
	s_nop 0
	v_addc_co_u32_e32 v7, vcc, 0, v5, vcc
	v_lshl_add_u64 v[2:3], v[2:3], 4, s[4:5]
	global_load_dwordx4 v[96:99], v[4:5], off
	global_load_dwordx4 v[100:103], v[4:5], off offset:1024
	global_load_dwordx4 v[104:107], v[4:5], off offset:2048
	global_load_dwordx4 v[108:111], v[4:5], off offset:3072
	global_load_dwordx4 v[112:115], v[6:7], off
	global_load_dwordx4 v[116:119], v[6:7], off offset:1024
	global_load_dwordx4 v[120:123], v[6:7], off offset:2048
	global_load_dwordx4 v[124:127], v[6:7], off offset:3072
	global_load_dwordx4 v[128:131], v[2:3], off
	global_load_dwordx4 v[132:135], v[2:3], off offset:1024
	global_load_dwordx4 v[136:139], v[2:3], off offset:2048
	global_load_dwordx4 v[140:143], v[2:3], off offset:3072
	v_add_co_u32_e32 v2, vcc, s6, v4
	s_lshl_b32 s3, s12, 4
	s_nop 0
	v_addc_co_u32_e32 v3, vcc, 0, v5, vcc
	global_load_dwordx4 v[144:147], v[2:3], off
	global_load_dwordx4 v[148:151], v[2:3], off offset:1024
	global_load_dwordx4 v[152:155], v[2:3], off offset:2048
	global_load_dwordx4 v[156:159], v[2:3], off offset:3072
	v_and_or_b32 v1, v0, 15, s3
	v_lshlrev_b32_e32 v1, 2, v1
	global_load_dword v179, v1, s[10:11]
	global_load_dword v180, v1, s[14:15]
	v_bfe_u32 v2, v0, 4, 2
	s_lshl_b32 s16, s3, 2
	v_lshl_add_u32 v2, v2, 4, s16
	global_load_dwordx4 v[228:231], v2, s[10:11]
	global_load_dwordx4 v[232:235], v2, s[14:15]
	v_cmp_gt_u32_e32 vcc, 32, v0
	v_lshlrev_b32_e32 v0, 2, v0
	s_and_saveexec_b64 s[4:5], vcc
	v_mov_b32_e32 v1, 0
	v_add_u32_e32 v2, 0xd000, v0
	ds_write2_b32 v2, v1, v1 offset0:176 offset1:208
	s_or_b64 exec, exec, s[4:5]
	global_load_dword v1, v0, s[8:9]
	global_load_dword v2, v0, s[8:9] offset:1024
	s_cmpk_gt_i32 s2, 0x61a
	s_waitcnt vmcnt(0)
	ds_write2st64_b32 v0, v1, v2 offset0:202 offset1:206
	s_waitcnt lgkmcnt(0)
	s_barrier
	s_cbranch_scc1 .LBB3_271
	s_load_dwordx8 s[56:63], s[0:1], 0x0
	s_load_dwordx4 s[4:7], s[0:1], 0x50
	s_mul_i32 s87, s12, 48
	s_lshl_b32 s66, s12, 9
	s_and_b32 s65, s13, 0xffffffc0
	s_lshl_b32 s86, s12, 3
	s_waitcnt lgkmcnt(0)
	v_writelane_b32 v226, s4, 0
	s_add_i32 s87, s87, 0xd200
	s_add_i32 s90, s66, 0xc200
	v_writelane_b32 v226, s5, 1
	v_writelane_b32 v226, s6, 2
	v_writelane_b32 v226, s7, 3
	s_lshl_b32 s4, s12, 12
	s_add_i32 s88, s4, 0x8200
	s_lshl_b32 s5, s12, 1
	s_load_dwordx2 s[72:73], s[0:1], 0x20
	s_load_dwordx2 s[76:77], s[0:1], 0x60
	s_add_u32 s0, s0, 0x68
	s_addc_u32 s1, s1, 0
	v_mbcnt_lo_u32_b32 v0, -1, 0
	v_writelane_b32 v226, s0, 4
	v_mbcnt_hi_u32_b32 v182, -1, v0
	s_mul_i32 s99, s12, 0x2080
	v_writelane_b32 v226, s1, 5
	s_or_b32 s0, s5, 1
	v_and_b32_e32 v0, 64, v182
	s_mov_b32 s91, 0xff800000
	s_lshl_b32 s95, s12, 8
	s_lshl_b32 s64, s0, 8
	s_lshl_b32 s98, s0, 7
	s_add_i32 s93, s4, 0x8500
	s_or_b32 s92, s99, 48
	s_mov_b32 s68, 0
	v_mov_b32_e32 v177, 0
	v_mov_b32_e32 v181, 0xff800000
	s_movk_i32 s69, 0x410
	v_xor_b32_e32 v183, 32, v182
	v_add_u32_e32 v184, 64, v0
	v_xor_b32_e32 v185, 4, v182
	v_xor_b32_e32 v186, 8, v182
	v_xor_b32_e32 v187, 16, v182
	v_mov_b32_e32 v188, 0x3c0
	v_writelane_b32 v226, s92, 6
	s_branch .LBB3_6
